# speedup vs baseline: 1.0102x; 1.0037x over previous
.Lmy_pc:
	s_add_u32 s8, s8, _Z6k_mainPKfPKDv8_DF16_S0_S3_S0_S0_S0_S0_S0_S0_S0_S0_S0_S3_S0_S0_S0_S0_S0_S0_S0_S0_S0_S0_S0_S0_S0_Pf-.Lmy_pc
	s_addc_u32 s9, s9, 0
	v_lshlrev_b32_e32 v9, 6, v0
	global_load_dword v10, v9, s[8:9]
	s_add_u32 s8, s8, 0x1000
	s_addc_u32 s9, s9, 0
	global_load_dword v11, v9, s[8:9]
	s_add_u32 s8, s8, 0x1000
	s_addc_u32 s9, s9, 0
	global_load_dword v12, v9, s[8:9]
	s_add_u32 s8, s8, 0x1000
	s_addc_u32 s9, s9, 0
	global_load_dword v13, v9, s[8:9]
.Lmy_nocodewarm:
	s_endpgm
	.section	.rodata,"a",@progbits
	.p2align	6, 0x0
